# HGRN2 chunk loop: the eight transpose reads for the state-delta MFMAs also issue before the third barrier (their data is final after the second), MFMA operands renamed to dead registers
# baseline (speedup 1.0000x reference)
.LBB0_302:
	v_lshlrev_b32_e32 v139, 2, v101
	v_add_u32_e32 v6, s26, v139
	v_lshl_add_u32 v2, v6, 2, 0
	v_add_u32_e32 v7, 0x10400, v2
	s_waitcnt lgkmcnt(0)
	s_barrier
	ds_read_b128 v[2:5], v7
	ds_read_b128 v[34:37], v7 offset:32
	ds_read_b128 v[38:41], v7 offset:64
	ds_read_b128 v[42:45], v7 offset:96
	v_lshlrev_b32_e32 v8, 4, v100
	v_and_b32_e32 v9, 0xf0, v8
	v_lshl_add_u32 v10, v100, 8, s27
	v_lshlrev_b32_e32 v6, 1, v6
	v_lshlrev_b32_e32 v58, 3, v100
	v_and_b32_e32 v60, 0xc0, v8
	v_lshl_add_u32 v59, v101, 8, v58
	v_and_or_b32 v58, v58, 24, v60
	v_lshlrev_b32_e32 v60, 1, v100
	v_and_b32_e32 v60, 32, v60
	v_and_b32_e32 v59, 0x100, v59
	v_or3_b32 v58, v58, v60, v59
	v_add_u32_e32 v59, s28, v58
	v_add_u32_e32 v60, s29, v58
	ds_read_b64_tr_b16 v[70:71], v59 offset:0
	ds_read_b64_tr_b16 v[72:73], v59 offset:0x800
	ds_read_b64_tr_b16 v[66:67], v59 offset:0x1000
	ds_read_b64_tr_b16 v[68:69], v59 offset:0x1800
	ds_read_b64_tr_b16 v[46:47], v60 offset:0
	ds_read_b64_tr_b16 v[48:49], v60 offset:0x800
	ds_read_b64_tr_b16 v[18:19], v60 offset:0x1000
	ds_read_b64_tr_b16 v[20:21], v60 offset:0x1800
	s_andn2_b64 vcc, exec, s[42:43]
	s_nop 0
	s_cbranch_vccz .Lhg_qpath
	s_waitcnt lgkmcnt(11)
	v_mul_f32_e32 v2, v84, v2
	v_mul_f32_e32 v3, v85, v3
	v_cvt_pk_bf16_f32 v2, v2, v3
	v_mul_f32_e32 v3, v86, v4
	v_mul_f32_e32 v4, v87, v5
	v_cvt_pk_bf16_f32 v3, v3, v4
	v_xad_u32 v4, v6, v9, v10
	ds_write_b64 v4, v[2:3] offset:32768
	s_waitcnt lgkmcnt(11)
	v_mul_f32_e32 v2, v88, v34
	v_mul_f32_e32 v3, v89, v35
	v_cvt_pk_bf16_f32 v2, v2, v3
	v_mul_f32_e32 v3, v90, v36
	v_mul_f32_e32 v4, v91, v37
	v_cvt_pk_bf16_f32 v3, v3, v4
	v_add_u32_e32 v4, 16, v6
	v_xad_u32 v4, v4, v9, v10
	ds_write_b64 v4, v[2:3] offset:32768
	s_waitcnt lgkmcnt(11)
	v_mul_f32_e32 v2, v92, v38
	v_mul_f32_e32 v3, v93, v39
	v_cvt_pk_bf16_f32 v2, v2, v3
	v_mul_f32_e32 v3, v94, v40
	v_mul_f32_e32 v4, v95, v41
	v_cvt_pk_bf16_f32 v3, v3, v4
	v_add_u32_e32 v4, 32, v6
	v_xad_u32 v4, v4, v9, v10
	ds_write_b64 v4, v[2:3] offset:32768
	s_waitcnt lgkmcnt(11)
	v_mul_f32_e32 v2, v96, v42
	v_mul_f32_e32 v3, v97, v43
	v_cvt_pk_bf16_f32 v2, v2, v3
	v_mul_f32_e32 v3, v98, v44
	v_mul_f32_e32 v4, v99, v45
	v_cvt_pk_bf16_f32 v3, v3, v4
	v_add_u32_e32 v4, 48, v6
	v_xad_u32 v4, v4, v9, v10
	ds_write_b64 v4, v[2:3] offset:32768
	s_waitcnt lgkmcnt(0)
	s_branch .Lhg_bar3
.Lhg_qpath:
	ds_read_b128 v[182:185], v105 offset:8192
	ds_read_b128 v[140:143], v105
	ds_read_b128 v[186:189], v106 offset:8192
	ds_read_b128 v[144:147], v106
	ds_read_b128 v[190:193], v107 offset:8192
	ds_read_b128 v[148:151], v107
	ds_read_b128 v[194:197], v108 offset:8192
	ds_read_b128 v[74:77], v108
	s_waitcnt lgkmcnt(15)
	v_mul_f32_e32 v2, v84, v2
	v_mul_f32_e32 v3, v85, v3
	v_cvt_pk_bf16_f32 v2, v2, v3
	v_mul_f32_e32 v3, v86, v4
	v_mul_f32_e32 v4, v87, v5
	v_cvt_pk_bf16_f32 v3, v3, v4
	v_xad_u32 v4, v6, v9, v10
	ds_write_b64 v4, v[2:3] offset:32768
	s_waitcnt lgkmcnt(15)
	v_mul_f32_e32 v2, v88, v34
	v_mul_f32_e32 v3, v89, v35
	v_cvt_pk_bf16_f32 v2, v2, v3
	v_mul_f32_e32 v3, v90, v36
	v_mul_f32_e32 v4, v91, v37
	v_cvt_pk_bf16_f32 v3, v3, v4
	v_add_u32_e32 v4, 16, v6
	v_xad_u32 v4, v4, v9, v10
	ds_write_b64 v4, v[2:3] offset:32768
	s_waitcnt lgkmcnt(15)
	v_mul_f32_e32 v2, v92, v38
	v_mul_f32_e32 v3, v93, v39
	v_cvt_pk_bf16_f32 v2, v2, v3
	v_mul_f32_e32 v3, v94, v40
	v_mul_f32_e32 v4, v95, v41
	v_cvt_pk_bf16_f32 v3, v3, v4
	v_add_u32_e32 v4, 32, v6
	v_xad_u32 v4, v4, v9, v10
	ds_write_b64 v4, v[2:3] offset:32768
	s_waitcnt lgkmcnt(15)
	v_mul_f32_e32 v2, v96, v42
	v_mul_f32_e32 v3, v97, v43
	v_cvt_pk_bf16_f32 v2, v2, v3
	v_mul_f32_e32 v3, v98, v44
	v_mul_f32_e32 v4, v99, v45
	v_cvt_pk_bf16_f32 v3, v3, v4
	v_add_u32_e32 v4, 48, v6
	v_xad_u32 v4, v4, v9, v10
	ds_write_b64 v4, v[2:3] offset:32768
	ds_read_b128 v[198:201], v109 offset:8192
	ds_read_b128 v[78:81], v109
	ds_read_b128 v[202:205], v110 offset:8192
	ds_read_b128 v[156:159], v110
	ds_read_b128 v[234:237], v111 offset:8192
	ds_read_b128 v[160:163], v111
	ds_read_b128 v[238:241], v112 offset:8192
	ds_read_b128 v[152:155], v112
	s_waitcnt lgkmcnt(8)
.Lhg_bar3:
	s_barrier
	v_lshlrev_b32_e32 v6, 4, v101
	v_add_u32_e32 v22, s33, v6
	v_add_u32_e32 v23, s46, v6
	v_mfma_f32_32x32x16_bf16 v[2:17], v[46:49], v[70:73], 0
	ds_read_b128 v[34:37], v22
	ds_read_b128 v[38:41], v22 offset:32
	ds_read_b128 v[58:61], v23
	ds_read_b128 v[54:57], v23 offset:32
	ds_read_b128 v[42:45], v22 offset:64
	ds_read_b128 v[50:53], v23 offset:64
	ds_read_b128 v[46:49], v22 offset:96
	ds_read_b128 v[62:65], v23 offset:96
	s_andn2_b64 vcc, exec, s[42:43]
	v_mfma_f32_32x32x16_bf16 v[2:17], v[18:21], v[66:69], v[2:17]
	s_cbranch_vccnz .LBB0_295
	v_cmp_le_i32_e32 vcc, v139, v100
	v_or_b32_e32 v172, 2, v139
	v_or_b32_e32 v173, 3, v139
	v_add_u32_e32 v174, 8, v139
	v_add_u32_e32 v175, 9, v139
	v_add_u32_e32 v176, 10, v139
	v_add_u32_e32 v177, 11, v139
	v_add_u32_e32 v178, 24, v139
	v_add_u32_e32 v179, 25, v139
	v_add_u32_e32 v180, 26, v139
	s_lshl_b32 s56, s7, 5
	s_cmp_gt_i32 s7, 7
	s_cselect_b32 s7, s90, 0xff
	s_sub_i32 s7, s7, s56
	s_and_b64 s[76:77], s[10:11], exec
	s_cselect_b32 s7, s56, s7
	s_add_i32 s76, s7, s3
	s_ashr_i32 s77, s76, 31
	s_lshl_b64 s[76:77], s[76:77], 11
	s_add_u32 s76, s47, s76
	s_addc_u32 s77, s52, s77
	v_add_u32_e32 v164, 16, v139
	v_add_u32_e32 v165, 17, v139
	v_add_u32_e32 v166, 18, v139
	v_add_u32_e32 v167, 19, v139
	s_waitcnt lgkmcnt(14)
	v_mfma_f32_32x32x16_bf16 v[18:33], v[182:185], v[140:143], 0
	s_waitcnt lgkmcnt(12)
	v_mfma_f32_32x32x16_bf16 v[18:33], v[186:189], v[144:147], v[18:33]
	s_waitcnt lgkmcnt(10)
	v_mfma_f32_32x32x16_bf16 v[18:33], v[190:193], v[148:151], v[18:33]
	s_waitcnt lgkmcnt(8)
	v_mfma_f32_32x32x16_bf16 v[18:33], v[194:197], v[74:77], v[18:33]
	s_waitcnt lgkmcnt(6)
	v_mfma_f32_32x32x16_bf16 v[18:33], v[198:201], v[78:81], v[18:33]
	s_waitcnt lgkmcnt(4)
	v_mfma_f32_32x32x16_bf16 v[18:33], v[202:205], v[156:159], v[18:33]
	s_waitcnt lgkmcnt(2)
	v_mfma_f32_32x32x16_bf16 v[18:33], v[234:237], v[160:163], v[18:33]
	s_waitcnt lgkmcnt(0)
	v_mfma_f32_32x32x16_bf16 v[18:33], v[238:241], v[152:155], v[18:33]
	v_add_u32_e32 v242, s27, v105
	ds_read_b128 v[182:185], v242 offset:32768
	v_add_u32_e32 v242, s27, v106
	ds_read_b128 v[186:189], v242 offset:32768
	v_add_u32_e32 v242, s27, v107
	ds_read_b128 v[190:193], v242 offset:32768
	v_add_u32_e32 v242, s27, v108
	ds_read_b128 v[194:197], v242 offset:32768
	v_add_u32_e32 v242, s27, v109
	ds_read_b128 v[198:201], v242 offset:32768
	v_add_u32_e32 v242, s27, v110
	ds_read_b128 v[202:205], v242 offset:32768
	v_add_u32_e32 v242, s27, v111
	ds_read_b128 v[234:237], v242 offset:32768
	v_add_u32_e32 v242, s27, v112
	ds_read_b128 v[238:241], v242 offset:32768
	v_cndmask_b32_e32 v18, 0, v18, vcc
	v_cmp_lt_i32_e32 vcc, v139, v100
	v_add_u32_e32 v139, 27, v139
	s_nop 0
	v_cndmask_b32_e32 v19, 0, v19, vcc
	v_cmp_le_i32_e32 vcc, v172, v100
	v_cvt_pk_bf16_f32 v18, v18, v19
	s_nop 1
	v_cndmask_b32_e32 v20, 0, v20, vcc
	v_cmp_le_i32_e32 vcc, v173, v100
	s_nop 1
	v_cndmask_b32_e32 v21, 0, v21, vcc
	v_cmp_le_i32_e32 vcc, v174, v100
	v_cvt_pk_bf16_f32 v19, v20, v21
	s_nop 1
	v_cndmask_b32_e32 v22, 0, v22, vcc
	v_cmp_le_i32_e32 vcc, v175, v100
	s_nop 1
	v_cndmask_b32_e32 v23, 0, v23, vcc
	v_cmp_le_i32_e32 vcc, v176, v100
	v_cvt_pk_bf16_f32 v20, v22, v23
	s_nop 0
	v_permlane32_swap_b32_e32 v18, v20
	v_cndmask_b32_e32 v24, 0, v24, vcc
	v_cmp_le_i32_e32 vcc, v177, v100
	s_nop 1
	v_cndmask_b32_e32 v25, 0, v25, vcc
	v_cmp_le_i32_e32 vcc, v164, v100
	v_cvt_pk_bf16_f32 v21, v24, v25
	s_nop 0
	v_permlane32_swap_b32_e32 v19, v21
	v_cndmask_b32_e32 v26, 0, v26, vcc
	v_cmp_le_i32_e32 vcc, v165, v100
	s_nop 1
	v_cndmask_b32_e32 v27, 0, v27, vcc
	v_cmp_le_i32_e32 vcc, v166, v100
	v_cvt_pk_bf16_f32 v164, v26, v27
	s_nop 1
	v_cndmask_b32_e32 v28, 0, v28, vcc
	v_cmp_le_i32_e32 vcc, v167, v100
	s_nop 1
	v_cndmask_b32_e32 v29, 0, v29, vcc
	v_cmp_le_i32_e32 vcc, v178, v100
	v_cvt_pk_bf16_f32 v165, v28, v29
	s_nop 1
	v_cndmask_b32_e32 v30, 0, v30, vcc
	v_cmp_le_i32_e32 vcc, v179, v100
	s_nop 1
	v_cndmask_b32_e32 v31, 0, v31, vcc
	v_cmp_le_i32_e32 vcc, v180, v100
	v_cvt_pk_bf16_f32 v166, v30, v31
	s_nop 0
	v_permlane32_swap_b32_e32 v164, v166
	v_cndmask_b32_e32 v32, 0, v32, vcc
	v_cmp_le_i32_e32 vcc, v139, v100
	v_add_u32_e32 v139, s27, v110
	s_nop 0
	v_cndmask_b32_e32 v33, 0, v33, vcc
	v_cvt_pk_bf16_f32 v167, v32, v33
	v_mfma_f32_32x32x16_bf16 v[18:33], v[18:21], v[70:73], 0
	v_permlane32_swap_b32_e32 v165, v167
	s_nop 1
	v_mfma_f32_32x32x16_bf16 v[18:33], v[164:167], v[66:69], v[18:33]
	s_waitcnt lgkmcnt(0)
	v_mfma_f32_32x32x16_bf16 v[18:33], v[140:143], v[182:185], v[18:33]
	v_mul_lo_u32 v140, s53, v101
	v_ashrrev_i32_e32 v141, 31, v140
	v_ashrrev_i32_e32 v101, 31, v100
	v_mfma_f32_32x32x16_bf16 v[18:33], v[144:147], v[186:189], v[18:33]
	v_mfma_f32_32x32x16_bf16 v[18:33], v[148:151], v[190:193], v[18:33]
	v_mfma_f32_32x32x16_bf16 v[18:33], v[74:77], v[194:197], v[18:33]
	v_mfma_f32_32x32x16_bf16 v[18:33], v[78:81], v[198:201], v[18:33]
	v_lshl_add_u64 v[66:67], v[140:141], 2, s[76:77]
	v_lshl_add_u64 v[74:75], v[100:101], 2, v[66:67]
	v_lshl_add_u64 v[76:77], s[62:63], 2, v[74:75]
	v_lshl_add_u64 v[78:79], v[76:77], 0, s[86:87]
	v_lshl_add_u64 v[80:81], v[78:79], 0, s[86:87]
	v_lshl_add_u64 v[100:101], v[80:81], 0, s[50:51]
	v_mfma_f32_32x32x16_bf16 v[18:33], v[156:159], v[202:205], v[18:33]
	v_lshl_add_u64 v[140:141], v[100:101], 0, s[86:87]
	v_mfma_f32_32x32x16_bf16 v[18:33], v[160:163], v[234:237], v[18:33]
	v_lshl_add_u64 v[66:67], v[140:141], 0, s[86:87]
	v_lshl_add_u64 v[68:69], v[66:67], 0, s[86:87]
	v_lshl_add_u64 v[142:143], v[68:69], 0, s[50:51]
	v_lshl_add_u64 v[144:145], v[142:143], 0, s[86:87]
	v_lshl_add_u64 v[146:147], v[144:145], 0, s[86:87]
	v_lshl_add_u64 v[148:149], v[146:147], 0, s[86:87]
	v_lshl_add_u64 v[150:151], v[148:149], 0, s[50:51]
	v_mfma_f32_32x32x16_bf16 v[18:33], v[152:155], v[238:241], v[18:33]
	s_nop 11
	global_store_dword v[74:75], v18, off
	global_store_dword v[76:77], v19, off
	global_store_dword v[78:79], v20, off
	global_store_dword v[80:81], v21, off
	global_store_dword v[100:101], v22, off
	global_store_dword v[140:141], v23, off
	global_store_dword v[66:67], v24, off
	global_store_dword v[68:69], v25, off
	global_store_dword v[142:143], v26, off
	global_store_dword v[144:145], v27, off
	global_store_dword v[146:147], v28, off
	global_store_dword v[148:149], v29, off
	global_store_dword v[150:151], v30, off
	v_lshl_add_u64 v[18:19], v[150:151], 0, s[86:87]
	global_store_dword v[18:19], v31, off
	v_lshl_add_u64 v[18:19], v[18:19], 0, s[86:87]
	global_store_dword v[18:19], v32, off
	v_lshl_add_u64 v[18:19], v[18:19], 0, s[86:87]
	global_store_dword v[18:19], v33, off
	s_branch .LBB0_295
